# speedup vs baseline: 1.0138x; 1.0015x over previous
.Lq2_nd0_1:
	v_mfma_scale_f32_32x32x64_f8f6f4 v[18:33], v[66:73], v[146:153], 0, v203, v203 op_sel_hi:[0,0,0]
	v_exp_f32_e64 v2, -v2
	v_exp_f32_e64 v3, -v3
	v_exp_f32_e64 v4, -v4
	v_exp_f32_e64 v5, -v5
	s_waitcnt lgkmcnt(0)
	v_add_co_u32_e64 v200, s[42:43], v200, v200
	v_add_co_u32_e64 v200, s[48:49], v200, v200
	v_add_co_u32_e64 v200, s[50:51], v200, v200
	v_add_co_u32_e64 v200, s[56:57], v200, v200
	v_add_f32_e32 v2, v2, v162
	v_add_f32_e32 v3, v3, v163
	v_add_f32_e32 v4, v4, v164
	v_add_f32_e32 v5, v5, v165
	s_mov_b64 exec, s[42:43]
	v_mul_f32_e32 v204, v204, v2
	s_mov_b64 exec, s[48:49]
	v_mul_f32_e32 v205, v205, v3
	s_mov_b64 exec, s[50:51]
	v_mul_f32_e32 v206, v206, v4
	s_mov_b64 exec, s[56:57]
	v_mul_f32_e32 v207, v207, v5
	s_mov_b64 exec, -1
	v_mfma_scale_f32_32x32x64_f8f6f4 v[18:33], v[74:81], v[154:161], v[18:33], v203, v203 op_sel_hi:[0,0,0]
	v_exp_f32_e64 v6, -v6
	v_exp_f32_e64 v7, -v7
	v_exp_f32_e64 v8, -v8
	v_exp_f32_e64 v9, -v9
	v_add_co_u32_e64 v200, s[42:43], v200, v200
	v_add_co_u32_e64 v200, s[48:49], v200, v200
	v_add_co_u32_e64 v200, s[50:51], v200, v200
	v_add_co_u32_e64 v200, s[56:57], v200, v200
	v_add_f32_e32 v6, v6, v166
	v_add_f32_e32 v7, v7, v167
	v_add_f32_e32 v8, v8, v168
	v_add_f32_e32 v9, v9, v169
	s_mov_b64 exec, s[42:43]
	v_mul_f32_e32 v208, v208, v6
	s_mov_b64 exec, s[48:49]
	v_mul_f32_e32 v209, v209, v7
	s_mov_b64 exec, s[50:51]
	v_mul_f32_e32 v210, v210, v8
	s_mov_b64 exec, s[56:57]
	v_mul_f32_e32 v211, v211, v9
	s_mov_b64 exec, -1
	v_mfma_scale_f32_32x32x64_f8f6f4 v[18:33], v[82:89], v[138:145], v[18:33], v203, v203 op_sel_hi:[0,0,0]
	v_exp_f32_e64 v10, -v10
	v_exp_f32_e64 v11, -v11
	v_exp_f32_e64 v12, -v12
	v_exp_f32_e64 v13, -v13
	v_add_co_u32_e64 v200, s[42:43], v200, v200
	v_add_co_u32_e64 v200, s[48:49], v200, v200
	v_add_co_u32_e64 v200, s[50:51], v200, v200
	v_add_co_u32_e64 v200, s[56:57], v200, v200
	v_add_f32_e32 v10, v10, v170
	v_add_f32_e32 v11, v11, v171
	v_add_f32_e32 v12, v12, v172
	v_add_f32_e32 v13, v13, v173
	s_mov_b64 exec, s[42:43]
	v_mul_f32_e32 v212, v212, v10
	s_mov_b64 exec, s[48:49]
	v_mul_f32_e32 v213, v213, v11
	s_mov_b64 exec, s[50:51]
	v_mul_f32_e32 v214, v214, v12
	s_mov_b64 exec, s[56:57]
	v_mul_f32_e32 v215, v215, v13
	s_mov_b64 exec, -1
	v_mfma_scale_f32_32x32x64_f8f6f4 v[18:33], v[90:97], v[130:137], v[18:33], v203, v203 op_sel_hi:[0,0,0]
	v_exp_f32_e64 v14, -v14
	v_exp_f32_e64 v15, -v15
	v_exp_f32_e64 v16, -v16
	v_exp_f32_e64 v17, -v17
	v_add_co_u32_e64 v200, s[42:43], v200, v200
	v_add_co_u32_e64 v200, s[48:49], v200, v200
	v_add_co_u32_e64 v200, s[50:51], v200, v200
	v_add_co_u32_e64 v200, s[56:57], v200, v200
	v_add_f32_e32 v14, v14, v174
	v_add_f32_e32 v15, v15, v175
	v_add_f32_e32 v16, v16, v176
	v_add_f32_e32 v17, v17, v177
	s_mov_b64 exec, s[42:43]
	v_mul_f32_e32 v216, v216, v14
	s_mov_b64 exec, s[48:49]
	v_mul_f32_e32 v217, v217, v15
	s_mov_b64 exec, s[50:51]
	v_mul_f32_e32 v218, v218, v16
	s_mov_b64 exec, s[56:57]
	v_mul_f32_e32 v219, v219, v17
	s_mov_b64 exec, -1
	s_cmp_lg_u32 s55, s40
	s_cbranch_scc1 .Lq2_nd1_1
	s_nop 15
	s_nop 7
	v_cndmask_b32_e64 v18, v18, v199, s[0:1]
	v_cndmask_b32_e64 v19, v19, v199, s[2:3]
	v_cndmask_b32_e64 v20, v20, v199, s[4:5]
	v_cndmask_b32_e64 v21, v21, v199, s[6:7]
	v_cndmask_b32_e64 v22, v22, v199, s[8:9]
	v_cndmask_b32_e64 v23, v23, v199, s[10:11]
	v_cndmask_b32_e64 v24, v24, v199, s[12:13]
	v_cndmask_b32_e64 v25, v25, v199, s[14:15]
	v_cndmask_b32_e64 v26, v26, v199, s[16:17]
	v_cndmask_b32_e64 v27, v27, v199, s[18:19]
	v_cndmask_b32_e64 v28, v28, v199, s[20:21]
	v_cndmask_b32_e64 v29, v29, v199, s[22:23]
	v_cndmask_b32_e64 v30, v30, v199, s[24:25]
	v_cndmask_b32_e64 v31, v31, v199, s[26:27]
	v_cndmask_b32_e64 v32, v32, v199, s[28:29]
	v_cndmask_b32_e64 v33, v33, v199, s[30:31]
.Lq2_nd1_1:
	s_nop 3
	s_waitcnt vmcnt(6)
	v_mfma_scale_f32_32x32x64_f8f6f4 v[2:17], v[34:41], v[106:113], 0, v203, v203 op_sel_hi:[0,0,0]
	v_exp_f32_e64 v18, -v18
	v_exp_f32_e64 v19, -v19
	v_exp_f32_e64 v20, -v20
	v_exp_f32_e64 v21, -v21
	v_add_co_u32_e64 v200, s[42:43], v200, v200
	v_add_co_u32_e64 v200, s[48:49], v200, v200
	v_add_co_u32_e64 v200, s[50:51], v200, v200
	v_add_co_u32_e64 v200, s[56:57], v200, v200
	v_add_f32_e32 v18, v18, v178
	v_add_f32_e32 v19, v19, v179
	v_add_f32_e32 v20, v20, v180
	v_add_f32_e32 v21, v21, v181
	s_mov_b64 exec, s[42:43]
	v_mul_f32_e32 v220, v220, v18
	s_mov_b64 exec, s[48:49]
	v_mul_f32_e32 v221, v221, v19
	s_mov_b64 exec, s[50:51]
	v_mul_f32_e32 v222, v222, v20
	s_mov_b64 exec, s[56:57]
	v_mul_f32_e32 v223, v223, v21
	s_mov_b64 exec, -1
	s_waitcnt vmcnt(4)
	v_mfma_scale_f32_32x32x64_f8f6f4 v[2:17], v[42:49], v[122:129], v[2:17], v203, v203 op_sel_hi:[0,0,0]
	v_exp_f32_e64 v22, -v22
	v_exp_f32_e64 v23, -v23
	v_exp_f32_e64 v24, -v24
	v_exp_f32_e64 v25, -v25
	v_add_co_u32_e64 v200, s[42:43], v200, v200
	v_add_co_u32_e64 v200, s[48:49], v200, v200
	v_add_co_u32_e64 v200, s[50:51], v200, v200
	v_add_co_u32_e64 v200, s[56:57], v200, v200
	v_add_f32_e32 v22, v22, v182
	v_add_f32_e32 v23, v23, v183
	v_add_f32_e32 v24, v24, v184
	v_add_f32_e32 v25, v25, v185
	s_mov_b64 exec, s[42:43]
	v_mul_f32_e32 v224, v224, v22
	s_mov_b64 exec, s[48:49]
	v_mul_f32_e32 v225, v225, v23
	s_mov_b64 exec, s[50:51]
	v_mul_f32_e32 v226, v226, v24
	s_mov_b64 exec, s[56:57]
	v_mul_f32_e32 v227, v227, v25
	s_mov_b64 exec, -1
	s_waitcnt vmcnt(2)
	v_mfma_scale_f32_32x32x64_f8f6f4 v[2:17], v[50:57], v[114:121], v[2:17], v203, v203 op_sel_hi:[0,0,0]
	v_exp_f32_e64 v26, -v26
	v_exp_f32_e64 v27, -v27
	v_exp_f32_e64 v28, -v28
	v_exp_f32_e64 v29, -v29
	v_add_co_u32_e64 v200, s[42:43], v200, v200
	v_add_co_u32_e64 v200, s[48:49], v200, v200
	v_add_co_u32_e64 v200, s[50:51], v200, v200
	v_add_co_u32_e64 v200, s[56:57], v200, v200
	v_add_f32_e32 v26, v26, v186
	v_add_f32_e32 v27, v27, v187
	v_add_f32_e32 v28, v28, v188
	v_add_f32_e32 v29, v29, v189
	s_mov_b64 exec, s[42:43]
	v_mul_f32_e32 v228, v228, v26
	s_mov_b64 exec, s[48:49]
	v_mul_f32_e32 v229, v229, v27
	s_mov_b64 exec, s[50:51]
	v_mul_f32_e32 v230, v230, v28
	s_mov_b64 exec, s[56:57]
	v_mul_f32_e32 v231, v231, v29
	s_mov_b64 exec, -1
	s_waitcnt vmcnt(0)
	v_mfma_scale_f32_32x32x64_f8f6f4 v[2:17], v[58:65], v[98:105], v[2:17], v203, v203 op_sel_hi:[0,0,0]
	v_exp_f32_e64 v30, -v30
	v_exp_f32_e64 v31, -v31
	v_exp_f32_e64 v32, -v32
	v_exp_f32_e64 v33, -v33
	v_add_co_u32_e64 v200, s[42:43], v200, v200
	v_add_co_u32_e64 v200, s[48:49], v200, v200
	v_add_co_u32_e64 v200, s[50:51], v200, v200
	v_add_co_u32_e64 v200, s[56:57], v200, v200
	v_add_f32_e32 v30, v30, v190
	v_add_f32_e32 v31, v31, v191
	v_add_f32_e32 v32, v32, v192
	v_add_f32_e32 v33, v33, v193
	s_mov_b64 exec, s[42:43]
	v_mul_f32_e32 v232, v232, v30
	s_mov_b64 exec, s[48:49]
	v_mul_f32_e32 v233, v233, v31
	s_mov_b64 exec, s[50:51]
	v_mul_f32_e32 v234, v234, v32
	s_mov_b64 exec, s[56:57]
	v_mul_f32_e32 v235, v235, v33
	s_mov_b64 exec, -1
	s_lshl_b32 s34, s39, 2
	s_add_i32 s34, s34, 2
	s_add_i32 s34, s34, s35
	s_and_b32 s41, s34, 15
	s_add_i32 s54, s34, 1
	s_and_b32 s54, s54, 15
	s_lshl_b32 s55, s41, 8
	s_lshl_b32 s38, s52, 12
	s_add_i32 s55, s55, s38
	v_lshl_add_u32 v236, v194, 2, s55
	ds_read_b32 v200, v236
	s_lshl_b32 s34, s54, 3
	s_add_i32 s34, s34, s52
	s_lshl_b32 s34, s34, 13
	s_add_i32 s34, s34, s53
	buffer_load_dwordx4 v[146:149], v195, s[44:47], s34 offen
	s_or_b32 s42, s34, 0x400
	buffer_load_dwordx4 v[150:153], v195, s[44:47], s42 offen
	s_or_b32 s43, s34, 0x800
	buffer_load_dwordx4 v[154:157], v195, s[44:47], s43 offen
	s_or_b32 s42, s34, 0xc00
	buffer_load_dwordx4 v[158:161], v195, s[44:47], s42 offen
	s_or_b32 s43, s34, 0x1000
	buffer_load_dwordx4 v[138:141], v195, s[44:47], s43 offen
	s_or_b32 s42, s34, 0x1400
	buffer_load_dwordx4 v[142:145], v195, s[44:47], s42 offen
	s_or_b32 s43, s34, 0x1800
	buffer_load_dwordx4 v[130:133], v195, s[44:47], s43 offen
	s_or_b32 s42, s34, 0x1c00
	buffer_load_dwordx4 v[134:137], v195, s[44:47], s42 offen
	s_lshl_b32 s55, s41, 3
	s_add_i32 s55, s55, s52
	s_cmp_lg_u32 s55, s33
	s_cbranch_scc1 .Lq2_nd0_2
	v_cndmask_b32_e64 v2, v2, v198, s[0:1]
	v_cndmask_b32_e64 v3, v3, v198, s[2:3]
	v_cndmask_b32_e64 v4, v4, v198, s[4:5]
	v_cndmask_b32_e64 v5, v5, v198, s[6:7]
	v_cndmask_b32_e64 v6, v6, v198, s[8:9]
	v_cndmask_b32_e64 v7, v7, v198, s[10:11]
	v_cndmask_b32_e64 v8, v8, v198, s[12:13]
	v_cndmask_b32_e64 v9, v9, v198, s[14:15]
	v_cndmask_b32_e64 v10, v10, v198, s[16:17]
	v_cndmask_b32_e64 v11, v11, v198, s[18:19]
	v_cndmask_b32_e64 v12, v12, v198, s[20:21]
	v_cndmask_b32_e64 v13, v13, v198, s[22:23]
	v_cndmask_b32_e64 v14, v14, v198, s[24:25]
	v_cndmask_b32_e64 v15, v15, v198, s[26:27]
	v_cndmask_b32_e64 v16, v16, v198, s[28:29]
	v_cndmask_b32_e64 v17, v17, v198, s[30:31]
.Lq2_nd0_2:
	v_mfma_scale_f32_32x32x64_f8f6f4 v[18:33], v[66:73], v[106:113], 0, v203, v203 op_sel_hi:[0,0,0]
	v_exp_f32_e64 v2, -v2
	v_exp_f32_e64 v3, -v3
	v_exp_f32_e64 v4, -v4
	v_exp_f32_e64 v5, -v5
	s_waitcnt lgkmcnt(0)
	v_add_co_u32_e64 v200, s[42:43], v200, v200
	v_add_co_u32_e64 v200, s[48:49], v200, v200
	v_add_co_u32_e64 v200, s[50:51], v200, v200
	v_add_co_u32_e64 v200, s[56:57], v200, v200
	v_add_f32_e32 v2, v2, v162
	v_add_f32_e32 v3, v3, v163
	v_add_f32_e32 v4, v4, v164
	v_add_f32_e32 v5, v5, v165
	s_mov_b64 exec, s[42:43]
	v_mul_f32_e32 v204, v204, v2
	s_mov_b64 exec, s[48:49]
	v_mul_f32_e32 v205, v205, v3
	s_mov_b64 exec, s[50:51]
	v_mul_f32_e32 v206, v206, v4
	s_mov_b64 exec, s[56:57]
	v_mul_f32_e32 v207, v207, v5
	s_mov_b64 exec, -1
	v_mfma_scale_f32_32x32x64_f8f6f4 v[18:33], v[74:81], v[122:129], v[18:33], v203, v203 op_sel_hi:[0,0,0]
	v_exp_f32_e64 v6, -v6
	v_exp_f32_e64 v7, -v7
	v_exp_f32_e64 v8, -v8
	v_exp_f32_e64 v9, -v9
	v_add_co_u32_e64 v200, s[42:43], v200, v200
	v_add_co_u32_e64 v200, s[48:49], v200, v200
	v_add_co_u32_e64 v200, s[50:51], v200, v200
	v_add_co_u32_e64 v200, s[56:57], v200, v200
	v_add_f32_e32 v6, v6, v166
	v_add_f32_e32 v7, v7, v167
	v_add_f32_e32 v8, v8, v168
	v_add_f32_e32 v9, v9, v169
	s_mov_b64 exec, s[42:43]
	v_mul_f32_e32 v208, v208, v6
	s_mov_b64 exec, s[48:49]
	v_mul_f32_e32 v209, v209, v7
	s_mov_b64 exec, s[50:51]
	v_mul_f32_e32 v210, v210, v8
	s_mov_b64 exec, s[56:57]
	v_mul_f32_e32 v211, v211, v9
	s_mov_b64 exec, -1
	v_mfma_scale_f32_32x32x64_f8f6f4 v[18:33], v[82:89], v[114:121], v[18:33], v203, v203 op_sel_hi:[0,0,0]
	v_exp_f32_e64 v10, -v10
	v_exp_f32_e64 v11, -v11
	v_exp_f32_e64 v12, -v12
	v_exp_f32_e64 v13, -v13
	v_add_co_u32_e64 v200, s[42:43], v200, v200
	v_add_co_u32_e64 v200, s[48:49], v200, v200
	v_add_co_u32_e64 v200, s[50:51], v200, v200
	v_add_co_u32_e64 v200, s[56:57], v200, v200
	v_add_f32_e32 v10, v10, v170
	v_add_f32_e32 v11, v11, v171
	v_add_f32_e32 v12, v12, v172
	v_add_f32_e32 v13, v13, v173
	s_mov_b64 exec, s[42:43]
	v_mul_f32_e32 v212, v212, v10
	s_mov_b64 exec, s[48:49]
	v_mul_f32_e32 v213, v213, v11
	s_mov_b64 exec, s[50:51]
	v_mul_f32_e32 v214, v214, v12
	s_mov_b64 exec, s[56:57]
	v_mul_f32_e32 v215, v215, v13
	s_mov_b64 exec, -1
	v_mfma_scale_f32_32x32x64_f8f6f4 v[18:33], v[90:97], v[98:105], v[18:33], v203, v203 op_sel_hi:[0,0,0]
	v_exp_f32_e64 v14, -v14
	v_exp_f32_e64 v15, -v15
	v_exp_f32_e64 v16, -v16
	v_exp_f32_e64 v17, -v17
	v_add_co_u32_e64 v200, s[42:43], v200, v200
	v_add_co_u32_e64 v200, s[48:49], v200, v200
	v_add_co_u32_e64 v200, s[50:51], v200, v200
	v_add_co_u32_e64 v200, s[56:57], v200, v200
	v_add_f32_e32 v14, v14, v174
	v_add_f32_e32 v15, v15, v175
	v_add_f32_e32 v16, v16, v176
	v_add_f32_e32 v17, v17, v177
	s_mov_b64 exec, s[42:43]
	v_mul_f32_e32 v216, v216, v14
	s_mov_b64 exec, s[48:49]
	v_mul_f32_e32 v217, v217, v15
	s_mov_b64 exec, s[50:51]
	v_mul_f32_e32 v218, v218, v16
	s_mov_b64 exec, s[56:57]
	v_mul_f32_e32 v219, v219, v17
	s_mov_b64 exec, -1
	s_cmp_lg_u32 s55, s40
	s_cbranch_scc1 .Lq2_nd1_2
	s_nop 15
	s_nop 7
	v_cndmask_b32_e64 v18, v18, v199, s[0:1]
	v_cndmask_b32_e64 v19, v19, v199, s[2:3]
	v_cndmask_b32_e64 v20, v20, v199, s[4:5]
	v_cndmask_b32_e64 v21, v21, v199, s[6:7]
	v_cndmask_b32_e64 v22, v22, v199, s[8:9]
	v_cndmask_b32_e64 v23, v23, v199, s[10:11]
	v_cndmask_b32_e64 v24, v24, v199, s[12:13]
	v_cndmask_b32_e64 v25, v25, v199, s[14:15]
	v_cndmask_b32_e64 v26, v26, v199, s[16:17]
	v_cndmask_b32_e64 v27, v27, v199, s[18:19]
	v_cndmask_b32_e64 v28, v28, v199, s[20:21]
	v_cndmask_b32_e64 v29, v29, v199, s[22:23]
	v_cndmask_b32_e64 v30, v30, v199, s[24:25]
	v_cndmask_b32_e64 v31, v31, v199, s[26:27]
	v_cndmask_b32_e64 v32, v32, v199, s[28:29]
	v_cndmask_b32_e64 v33, v33, v199, s[30:31]
.Lq2_nd1_2:
	s_nop 3
	s_waitcnt vmcnt(6)
	v_mfma_scale_f32_32x32x64_f8f6f4 v[2:17], v[34:41], v[146:153], 0, v203, v203 op_sel_hi:[0,0,0]
	v_exp_f32_e64 v18, -v18
	v_exp_f32_e64 v19, -v19
	v_exp_f32_e64 v20, -v20
	v_exp_f32_e64 v21, -v21
	v_add_co_u32_e64 v200, s[42:43], v200, v200
	v_add_co_u32_e64 v200, s[48:49], v200, v200
	v_add_co_u32_e64 v200, s[50:51], v200, v200
	v_add_co_u32_e64 v200, s[56:57], v200, v200
	v_add_f32_e32 v18, v18, v178
	v_add_f32_e32 v19, v19, v179
	v_add_f32_e32 v20, v20, v180
	v_add_f32_e32 v21, v21, v181
	s_mov_b64 exec, s[42:43]
	v_mul_f32_e32 v220, v220, v18
	s_mov_b64 exec, s[48:49]
	v_mul_f32_e32 v221, v221, v19
	s_mov_b64 exec, s[50:51]
	v_mul_f32_e32 v222, v222, v20
	s_mov_b64 exec, s[56:57]
	v_mul_f32_e32 v223, v223, v21
	s_mov_b64 exec, -1
	s_waitcnt vmcnt(4)
	v_mfma_scale_f32_32x32x64_f8f6f4 v[2:17], v[42:49], v[154:161], v[2:17], v203, v203 op_sel_hi:[0,0,0]
	v_exp_f32_e64 v22, -v22
	v_exp_f32_e64 v23, -v23
	v_exp_f32_e64 v24, -v24
	v_exp_f32_e64 v25, -v25
	v_add_co_u32_e64 v200, s[42:43], v200, v200
	v_add_co_u32_e64 v200, s[48:49], v200, v200
	v_add_co_u32_e64 v200, s[50:51], v200, v200
	v_add_co_u32_e64 v200, s[56:57], v200, v200
	v_add_f32_e32 v22, v22, v182
	v_add_f32_e32 v23, v23, v183
	v_add_f32_e32 v24, v24, v184
	v_add_f32_e32 v25, v25, v185
	s_mov_b64 exec, s[42:43]
	v_mul_f32_e32 v224, v224, v22
	s_mov_b64 exec, s[48:49]
	v_mul_f32_e32 v225, v225, v23
	s_mov_b64 exec, s[50:51]
	v_mul_f32_e32 v226, v226, v24
	s_mov_b64 exec, s[56:57]
	v_mul_f32_e32 v227, v227, v25
	s_mov_b64 exec, -1
	s_waitcnt vmcnt(2)
	v_mfma_scale_f32_32x32x64_f8f6f4 v[2:17], v[50:57], v[138:145], v[2:17], v203, v203 op_sel_hi:[0,0,0]
	v_exp_f32_e64 v26, -v26
	v_exp_f32_e64 v27, -v27
	v_exp_f32_e64 v28, -v28
	v_exp_f32_e64 v29, -v29
	v_add_co_u32_e64 v200, s[42:43], v200, v200
	v_add_co_u32_e64 v200, s[48:49], v200, v200
	v_add_co_u32_e64 v200, s[50:51], v200, v200
	v_add_co_u32_e64 v200, s[56:57], v200, v200
	v_add_f32_e32 v26, v26, v186
	v_add_f32_e32 v27, v27, v187
	v_add_f32_e32 v28, v28, v188
	v_add_f32_e32 v29, v29, v189
	s_mov_b64 exec, s[42:43]
	v_mul_f32_e32 v228, v228, v26
	s_mov_b64 exec, s[48:49]
	v_mul_f32_e32 v229, v229, v27
	s_mov_b64 exec, s[50:51]
	v_mul_f32_e32 v230, v230, v28
	s_mov_b64 exec, s[56:57]
	v_mul_f32_e32 v231, v231, v29
	s_mov_b64 exec, -1
	s_waitcnt vmcnt(0)
	v_mfma_scale_f32_32x32x64_f8f6f4 v[2:17], v[58:65], v[130:137], v[2:17], v203, v203 op_sel_hi:[0,0,0]
	v_exp_f32_e64 v30, -v30
	v_exp_f32_e64 v31, -v31
	v_exp_f32_e64 v32, -v32
	v_exp_f32_e64 v33, -v33
	v_add_co_u32_e64 v200, s[42:43], v200, v200
	v_add_co_u32_e64 v200, s[48:49], v200, v200
	v_add_co_u32_e64 v200, s[50:51], v200, v200
	v_add_co_u32_e64 v200, s[56:57], v200, v200
	v_add_f32_e32 v30, v30, v190
	v_add_f32_e32 v31, v31, v191
	v_add_f32_e32 v32, v32, v192
	v_add_f32_e32 v33, v33, v193
	s_mov_b64 exec, s[42:43]
	v_mul_f32_e32 v232, v232, v30
	s_mov_b64 exec, s[48:49]
	v_mul_f32_e32 v233, v233, v31
	s_mov_b64 exec, s[50:51]
	v_mul_f32_e32 v234, v234, v32
	s_mov_b64 exec, s[56:57]
	v_mul_f32_e32 v235, v235, v33
	s_mov_b64 exec, -1
	s_lshl_b32 s34, s39, 2
	s_add_i32 s34, s34, 3
	s_add_i32 s34, s34, s35
	s_and_b32 s41, s34, 15
	s_add_i32 s54, s34, 1
	s_and_b32 s54, s54, 15
	s_lshl_b32 s55, s41, 8
	s_lshl_b32 s38, s52, 12
	s_add_i32 s55, s55, s38
	v_lshl_add_u32 v236, v194, 2, s55
	ds_read_b32 v200, v236
	s_lshl_b32 s34, s54, 3
	s_add_i32 s34, s34, s52
	s_lshl_b32 s34, s34, 13
	s_add_i32 s34, s34, s53
	buffer_load_dwordx4 v[106:109], v195, s[44:47], s34 offen
	s_or_b32 s42, s34, 0x400
	buffer_load_dwordx4 v[110:113], v195, s[44:47], s42 offen
	s_or_b32 s43, s34, 0x800
	buffer_load_dwordx4 v[122:125], v195, s[44:47], s43 offen
	s_or_b32 s42, s34, 0xc00
	buffer_load_dwordx4 v[126:129], v195, s[44:47], s42 offen
	s_or_b32 s43, s34, 0x1000
	buffer_load_dwordx4 v[114:117], v195, s[44:47], s43 offen
	s_or_b32 s42, s34, 0x1400
	buffer_load_dwordx4 v[118:121], v195, s[44:47], s42 offen
	s_or_b32 s43, s34, 0x1800
	buffer_load_dwordx4 v[98:101], v195, s[44:47], s43 offen
	s_or_b32 s42, s34, 0x1c00
	buffer_load_dwordx4 v[102:105], v195, s[44:47], s42 offen
	s_lshl_b32 s55, s41, 3
	s_add_i32 s55, s55, s52
	s_cmp_lg_u32 s55, s33
	s_cbranch_scc1 .Lq2_nd0_3
	v_cndmask_b32_e64 v2, v2, v198, s[0:1]
	v_cndmask_b32_e64 v3, v3, v198, s[2:3]
	v_cndmask_b32_e64 v4, v4, v198, s[4:5]
	v_cndmask_b32_e64 v5, v5, v198, s[6:7]
	v_cndmask_b32_e64 v6, v6, v198, s[8:9]
	v_cndmask_b32_e64 v7, v7, v198, s[10:11]
	v_cndmask_b32_e64 v8, v8, v198, s[12:13]
	v_cndmask_b32_e64 v9, v9, v198, s[14:15]
	v_cndmask_b32_e64 v10, v10, v198, s[16:17]
	v_cndmask_b32_e64 v11, v11, v198, s[18:19]
	v_cndmask_b32_e64 v12, v12, v198, s[20:21]
	v_cndmask_b32_e64 v13, v13, v198, s[22:23]
	v_cndmask_b32_e64 v14, v14, v198, s[24:25]
	v_cndmask_b32_e64 v15, v15, v198, s[26:27]
	v_cndmask_b32_e64 v16, v16, v198, s[28:29]
	v_cndmask_b32_e64 v17, v17, v198, s[30:31]
.Lq2_nd0_3:
	v_mfma_scale_f32_32x32x64_f8f6f4 v[18:33], v[66:73], v[146:153], 0, v203, v203 op_sel_hi:[0,0,0]
	ds_read_b128 v[236:239], v202
	v_exp_f32_e64 v2, -v2
	v_exp_f32_e64 v3, -v3
	v_exp_f32_e64 v4, -v4
	v_exp_f32_e64 v5, -v5
	s_waitcnt lgkmcnt(1)
	v_add_co_u32_e64 v200, s[42:43], v200, v200
	v_add_co_u32_e64 v200, s[48:49], v200, v200
	v_add_co_u32_e64 v200, s[50:51], v200, v200
	v_add_co_u32_e64 v200, s[56:57], v200, v200
	v_add_f32_e32 v2, v2, v162
	v_add_f32_e32 v3, v3, v163
	v_add_f32_e32 v4, v4, v164
	v_add_f32_e32 v5, v5, v165
	s_mov_b64 exec, s[42:43]
	v_mul_f32_e32 v204, v204, v2
	s_mov_b64 exec, s[48:49]
	v_mul_f32_e32 v205, v205, v3
	s_mov_b64 exec, s[50:51]
	v_mul_f32_e32 v206, v206, v4
	s_mov_b64 exec, s[56:57]
	v_mul_f32_e32 v207, v207, v5
	s_mov_b64 exec, -1
	v_log_f32_e32 v2, v204
	v_log_f32_e32 v3, v205
	v_log_f32_e32 v4, v206
	v_log_f32_e32 v5, v207
	s_waitcnt lgkmcnt(0)
	v_fmac_f32_e32 v201, v2, v236
	v_fmac_f32_e32 v201, v3, v237
	v_fmac_f32_e32 v201, v4, v238
	v_fmac_f32_e32 v201, v5, v239
	v_mfma_scale_f32_32x32x64_f8f6f4 v[18:33], v[74:81], v[154:161], v[18:33], v203, v203 op_sel_hi:[0,0,0]
	ds_read_b128 v[236:239], v202 offset:16
	v_exp_f32_e64 v6, -v6
	v_exp_f32_e64 v7, -v7
	v_exp_f32_e64 v8, -v8
	v_exp_f32_e64 v9, -v9
	v_add_co_u32_e64 v200, s[42:43], v200, v200
	v_add_co_u32_e64 v200, s[48:49], v200, v200
	v_add_co_u32_e64 v200, s[50:51], v200, v200
	v_add_co_u32_e64 v200, s[56:57], v200, v200
	v_add_f32_e32 v6, v6, v166
	v_add_f32_e32 v7, v7, v167
	v_add_f32_e32 v8, v8, v168
	v_add_f32_e32 v9, v9, v169
	s_mov_b64 exec, s[42:43]
	v_mul_f32_e32 v208, v208, v6
	s_mov_b64 exec, s[48:49]
	v_mul_f32_e32 v209, v209, v7
	s_mov_b64 exec, s[50:51]
	v_mul_f32_e32 v210, v210, v8
	s_mov_b64 exec, s[56:57]
	v_mul_f32_e32 v211, v211, v9
	s_mov_b64 exec, -1
	v_log_f32_e32 v6, v208
	v_log_f32_e32 v7, v209
	v_log_f32_e32 v8, v210
	v_log_f32_e32 v9, v211
	s_waitcnt lgkmcnt(0)
	v_fmac_f32_e32 v201, v6, v236
	v_fmac_f32_e32 v201, v7, v237
	v_fmac_f32_e32 v201, v8, v238
	v_fmac_f32_e32 v201, v9, v239
	v_mfma_scale_f32_32x32x64_f8f6f4 v[18:33], v[82:89], v[138:145], v[18:33], v203, v203 op_sel_hi:[0,0,0]
	ds_read_b128 v[236:239], v202 offset:32
	v_exp_f32_e64 v10, -v10
	v_exp_f32_e64 v11, -v11
	v_exp_f32_e64 v12, -v12
	v_exp_f32_e64 v13, -v13
	v_add_co_u32_e64 v200, s[42:43], v200, v200
	v_add_co_u32_e64 v200, s[48:49], v200, v200
	v_add_co_u32_e64 v200, s[50:51], v200, v200
	v_add_co_u32_e64 v200, s[56:57], v200, v200
	v_add_f32_e32 v10, v10, v170
	v_add_f32_e32 v11, v11, v171
	v_add_f32_e32 v12, v12, v172
	v_add_f32_e32 v13, v13, v173
	s_mov_b64 exec, s[42:43]
	v_mul_f32_e32 v212, v212, v10
	s_mov_b64 exec, s[48:49]
	v_mul_f32_e32 v213, v213, v11
	s_mov_b64 exec, s[50:51]
	v_mul_f32_e32 v214, v214, v12
	s_mov_b64 exec, s[56:57]
	v_mul_f32_e32 v215, v215, v13
	s_mov_b64 exec, -1
	v_log_f32_e32 v10, v212
	v_log_f32_e32 v11, v213
	v_log_f32_e32 v12, v214
	v_log_f32_e32 v13, v215
	s_waitcnt lgkmcnt(0)
	v_fmac_f32_e32 v201, v10, v236
	v_fmac_f32_e32 v201, v11, v237
	v_fmac_f32_e32 v201, v12, v238
	v_fmac_f32_e32 v201, v13, v239
	v_mfma_scale_f32_32x32x64_f8f6f4 v[18:33], v[90:97], v[130:137], v[18:33], v203, v203 op_sel_hi:[0,0,0]
	ds_read_b128 v[236:239], v202 offset:48
	v_exp_f32_e64 v14, -v14
	v_exp_f32_e64 v15, -v15
	v_exp_f32_e64 v16, -v16
	v_exp_f32_e64 v17, -v17
	v_add_co_u32_e64 v200, s[42:43], v200, v200
	v_add_co_u32_e64 v200, s[48:49], v200, v200
	v_add_co_u32_e64 v200, s[50:51], v200, v200
	v_add_co_u32_e64 v200, s[56:57], v200, v200
	v_add_f32_e32 v14, v14, v174
	v_add_f32_e32 v15, v15, v175
	v_add_f32_e32 v16, v16, v176
	v_add_f32_e32 v17, v17, v177
	s_mov_b64 exec, s[42:43]
	v_mul_f32_e32 v216, v216, v14
	s_mov_b64 exec, s[48:49]
	v_mul_f32_e32 v217, v217, v15
	s_mov_b64 exec, s[50:51]
	v_mul_f32_e32 v218, v218, v16
	s_mov_b64 exec, s[56:57]
	v_mul_f32_e32 v219, v219, v17
	s_mov_b64 exec, -1
	v_log_f32_e32 v14, v216
	v_log_f32_e32 v15, v217
	v_log_f32_e32 v16, v218
	v_log_f32_e32 v17, v219
	s_waitcnt lgkmcnt(0)
	v_fmac_f32_e32 v201, v14, v236
	v_fmac_f32_e32 v201, v15, v237
	v_fmac_f32_e32 v201, v16, v238
	v_fmac_f32_e32 v201, v17, v239
	s_cmp_lg_u32 s55, s40
	s_cbranch_scc1 .Lq2_nd1_3
	s_nop 15
	s_nop 7
	v_cndmask_b32_e64 v18, v18, v199, s[0:1]
	v_cndmask_b32_e64 v19, v19, v199, s[2:3]
	v_cndmask_b32_e64 v20, v20, v199, s[4:5]
	v_cndmask_b32_e64 v21, v21, v199, s[6:7]
	v_cndmask_b32_e64 v22, v22, v199, s[8:9]
	v_cndmask_b32_e64 v23, v23, v199, s[10:11]
	v_cndmask_b32_e64 v24, v24, v199, s[12:13]
	v_cndmask_b32_e64 v25, v25, v199, s[14:15]
	v_cndmask_b32_e64 v26, v26, v199, s[16:17]
	v_cndmask_b32_e64 v27, v27, v199, s[18:19]
	v_cndmask_b32_e64 v28, v28, v199, s[20:21]
	v_cndmask_b32_e64 v29, v29, v199, s[22:23]
	v_cndmask_b32_e64 v30, v30, v199, s[24:25]
	v_cndmask_b32_e64 v31, v31, v199, s[26:27]
	v_cndmask_b32_e64 v32, v32, v199, s[28:29]
	v_cndmask_b32_e64 v33, v33, v199, s[30:31]
.Lq2_nd1_3:
	s_nop 3
	s_waitcnt vmcnt(6)
	v_mfma_scale_f32_32x32x64_f8f6f4 v[2:17], v[34:41], v[106:113], 0, v203, v203 op_sel_hi:[0,0,0]
	ds_read_b128 v[236:239], v202 offset:64
	v_exp_f32_e64 v18, -v18
	v_exp_f32_e64 v19, -v19
	v_exp_f32_e64 v20, -v20
	v_exp_f32_e64 v21, -v21
	v_add_co_u32_e64 v200, s[42:43], v200, v200
	v_add_co_u32_e64 v200, s[48:49], v200, v200
	v_add_co_u32_e64 v200, s[50:51], v200, v200
	v_add_co_u32_e64 v200, s[56:57], v200, v200
	v_add_f32_e32 v18, v18, v178
	v_add_f32_e32 v19, v19, v179
	v_add_f32_e32 v20, v20, v180
	v_add_f32_e32 v21, v21, v181
	s_mov_b64 exec, s[42:43]
	v_mul_f32_e32 v220, v220, v18
	s_mov_b64 exec, s[48:49]
	v_mul_f32_e32 v221, v221, v19
	s_mov_b64 exec, s[50:51]
	v_mul_f32_e32 v222, v222, v20
	s_mov_b64 exec, s[56:57]
	v_mul_f32_e32 v223, v223, v21
	s_mov_b64 exec, -1
	v_log_f32_e32 v18, v220
	v_log_f32_e32 v19, v221
	v_log_f32_e32 v20, v222
	v_log_f32_e32 v21, v223
	s_waitcnt lgkmcnt(0)
	v_fmac_f32_e32 v201, v18, v236
	v_fmac_f32_e32 v201, v19, v237
	v_fmac_f32_e32 v201, v20, v238
	v_fmac_f32_e32 v201, v21, v239
	s_waitcnt vmcnt(4)
	v_mfma_scale_f32_32x32x64_f8f6f4 v[2:17], v[42:49], v[122:129], v[2:17], v203, v203 op_sel_hi:[0,0,0]
	ds_read_b128 v[236:239], v202 offset:80
	v_exp_f32_e64 v22, -v22
	v_exp_f32_e64 v23, -v23
	v_exp_f32_e64 v24, -v24
	v_exp_f32_e64 v25, -v25
	v_add_co_u32_e64 v200, s[42:43], v200, v200
	v_add_co_u32_e64 v200, s[48:49], v200, v200
	v_add_co_u32_e64 v200, s[50:51], v200, v200
	v_add_co_u32_e64 v200, s[56:57], v200, v200
	v_add_f32_e32 v22, v22, v182
	v_add_f32_e32 v23, v23, v183
	v_add_f32_e32 v24, v24, v184
	v_add_f32_e32 v25, v25, v185
	s_mov_b64 exec, s[42:43]
	v_mul_f32_e32 v224, v224, v22
	s_mov_b64 exec, s[48:49]
	v_mul_f32_e32 v225, v225, v23
	s_mov_b64 exec, s[50:51]
	v_mul_f32_e32 v226, v226, v24
	s_mov_b64 exec, s[56:57]
	v_mul_f32_e32 v227, v227, v25
	s_mov_b64 exec, -1
	v_log_f32_e32 v22, v224
	v_log_f32_e32 v23, v225
	v_log_f32_e32 v24, v226
	v_log_f32_e32 v25, v227
	s_waitcnt lgkmcnt(0)
	v_fmac_f32_e32 v201, v22, v236
	v_fmac_f32_e32 v201, v23, v237
	v_fmac_f32_e32 v201, v24, v238
	v_fmac_f32_e32 v201, v25, v239
	s_waitcnt vmcnt(2)
	v_mfma_scale_f32_32x32x64_f8f6f4 v[2:17], v[50:57], v[114:121], v[2:17], v203, v203 op_sel_hi:[0,0,0]
	ds_read_b128 v[236:239], v202 offset:96
	v_exp_f32_e64 v26, -v26
	v_exp_f32_e64 v27, -v27
	v_exp_f32_e64 v28, -v28
	v_exp_f32_e64 v29, -v29
	v_add_co_u32_e64 v200, s[42:43], v200, v200
	v_add_co_u32_e64 v200, s[48:49], v200, v200
	v_add_co_u32_e64 v200, s[50:51], v200, v200
	v_add_co_u32_e64 v200, s[56:57], v200, v200
	v_add_f32_e32 v26, v26, v186
	v_add_f32_e32 v27, v27, v187
	v_add_f32_e32 v28, v28, v188
	v_add_f32_e32 v29, v29, v189
	s_mov_b64 exec, s[42:43]
	v_mul_f32_e32 v228, v228, v26
	s_mov_b64 exec, s[48:49]
	v_mul_f32_e32 v229, v229, v27
	s_mov_b64 exec, s[50:51]
	v_mul_f32_e32 v230, v230, v28
	s_mov_b64 exec, s[56:57]
	v_mul_f32_e32 v231, v231, v29
	s_mov_b64 exec, -1
	v_log_f32_e32 v26, v228
	v_log_f32_e32 v27, v229
	v_log_f32_e32 v28, v230
	v_log_f32_e32 v29, v231
	s_waitcnt lgkmcnt(0)
	v_fmac_f32_e32 v201, v26, v236
	v_fmac_f32_e32 v201, v27, v237
	v_fmac_f32_e32 v201, v28, v238
	v_fmac_f32_e32 v201, v29, v239
	s_waitcnt vmcnt(0)
	v_mfma_scale_f32_32x32x64_f8f6f4 v[2:17], v[58:65], v[98:105], v[2:17], v203, v203 op_sel_hi:[0,0,0]
	ds_read_b128 v[236:239], v202 offset:112
	v_exp_f32_e64 v30, -v30
	v_exp_f32_e64 v31, -v31
	v_exp_f32_e64 v32, -v32
	v_exp_f32_e64 v33, -v33
	v_add_co_u32_e64 v200, s[42:43], v200, v200
	v_add_co_u32_e64 v200, s[48:49], v200, v200
	v_add_co_u32_e64 v200, s[50:51], v200, v200
	v_add_co_u32_e64 v200, s[56:57], v200, v200
	v_add_f32_e32 v30, v30, v190
	v_add_f32_e32 v31, v31, v191
	v_add_f32_e32 v32, v32, v192
	v_add_f32_e32 v33, v33, v193
	s_mov_b64 exec, s[42:43]
	v_mul_f32_e32 v232, v232, v30
	s_mov_b64 exec, s[48:49]
	v_mul_f32_e32 v233, v233, v31
	s_mov_b64 exec, s[50:51]
	v_mul_f32_e32 v234, v234, v32
	s_mov_b64 exec, s[56:57]
	v_mul_f32_e32 v235, v235, v33
	s_mov_b64 exec, -1
	v_log_f32_e32 v30, v232
	v_log_f32_e32 v31, v233
	v_log_f32_e32 v32, v234
	v_log_f32_e32 v33, v235
	s_waitcnt lgkmcnt(0)
	v_fmac_f32_e32 v201, v30, v236
	v_fmac_f32_e32 v201, v31, v237
	v_fmac_f32_e32 v201, v32, v238
	v_fmac_f32_e32 v201, v33, v239
	s_add_i32 s39, s39, 1
	s_cmp_lt_u32 s39, 4
	s_cbranch_scc1 .Lq2_loop
